# P9 token loop: next token's expert ids/ranks/weights loaded one iteration ahead; H-row conversions wait at the YR stage
# baseline (speedup 1.0000x reference)
; __device__ __forceinline__ float bf_lo(unsigned u) { return __uint_as_float(u << 16); }
; __device__ __forceinline__ float bf_hi(unsigned u) { return __uint_as_float(u & 0xffff0000u); }
; __device__ __forceinline__ void p9_final(Ctx& X) {
;     ...
;     const int gw = X.bid * NWAVES + X.wave, NGW = X.G * NWAVES, lane = X.lane;
;     for (int t = gw; t < T; t += NGW) {
;         const u32x2* hr = (const u32x2*)(XP_Hh(X) + (size_t)t * D) + lane;
;         f32x4 v[8];
; #pragma unroll
;         for (int j = 0; j < 8; ++j) { const u32x2 hv = hr[64 * j]; v[j] = (f32x4){bf_lo(hv.x), bf_hi(hv.x), bf_lo(hv.y), bf_hi(hv.y)}; }
; #pragma unroll
;         for (int k = 0; k < 4; ++k) { const int e = XP_TOPI(X)[t * 4 + k], r = XP_TOPR(X)[t * 4 + k]; const float wk = XP_TOPW(X)[t * 4 + k];
;             const unsigned* yr = (const unsigned*)(XP_YR(X) + ((size_t)tab[8 + e] * 256 + r) * D) + lane;
.LBB0_1126:
	s_lshl_b32 s2, s87, 3
	s_add_i32 s2, s93, s2
	s_cmpk_gt_i32 s2, 0x1fff
	s_cbranch_scc1 .LBB0_1129
	v_mbcnt_lo_u32_b32 v0, -1, 0
	v_mbcnt_hi_u32_b32 v0, -1, v0
	v_and_b32_e32 v1, 64, v0
	v_add_u32_e32 v1, 64, v1
	v_xor_b32_e32 v2, 1, v0
	v_cmp_lt_i32_e32 vcc, v2, v1
	s_lshl_b32 s4, s92, 3
	s_add_u32 s12, s90, 0x2e00000
	v_cndmask_b32_e32 v2, v0, v2, vcc
	v_lshlrev_b32_e32 v29, 2, v2
	v_xor_b32_e32 v2, 2, v0
	v_cmp_lt_i32_e32 vcc, v2, v1
	s_load_dwordx2 s[6:7], s[0:1], 0x90
	s_addc_u32 s13, s91, 0
	v_cndmask_b32_e32 v2, v0, v2, vcc
	v_lshlrev_b32_e32 v48, 2, v2
	v_xor_b32_e32 v2, 4, v0
	v_cmp_lt_i32_e32 vcc, v2, v1
	s_add_u32 s14, s90, 0x2e20000
	s_addc_u32 s15, s91, 0
	v_cndmask_b32_e32 v2, v0, v2, vcc
	v_lshlrev_b32_e32 v49, 2, v2
	v_xor_b32_e32 v2, 8, v0
	v_cmp_lt_i32_e32 vcc, v2, v1
	v_mov_b32_e32 v5, 0
	s_add_u32 s16, s90, 0x2e40000
	v_cndmask_b32_e32 v2, v0, v2, vcc
	v_lshlrev_b32_e32 v4, 4, v194
	v_lshlrev_b32_e32 v50, 2, v2
	v_xor_b32_e32 v2, 16, v0
	s_addc_u32 s17, s91, 0
	s_waitcnt lgkmcnt(0)
	v_lshl_add_u64 v[6:7], s[6:7], 0, v[4:5]
	s_mov_b64 s[6:7], 0x1400
	v_cmp_lt_i32_e32 vcc, v2, v1
	s_add_u32 s0, s90, 0x26000000
	v_lshl_add_u64 v[10:11], v[6:7], 0, s[6:7]
	s_mov_b64 s[6:7], 0x1800
	v_cndmask_b32_e32 v2, v0, v2, vcc
	s_addc_u32 s1, s91, 0
	v_lshl_add_u64 v[12:13], v[6:7], 0, s[6:7]
	s_mov_b64 s[6:7], 0x1c00
	s_lshl_b32 s3, s87, 5
	s_lshl_b32 s5, s93, 2
	v_lshlrev_b32_e32 v51, 2, v2
	v_xor_b32_e32 v2, 32, v0
	v_lshl_add_u64 v[14:15], v[6:7], 0, s[6:7]
	s_add_i32 s6, s3, s5
	s_ashr_i32 s3, s2, 31
	v_cmp_lt_i32_e32 vcc, v2, v1
	s_lshl_b32 s18, s92, 5
	s_lshl_b64 s[8:9], s[2:3], 12
	v_cndmask_b32_e32 v0, v0, v2, vcc
	s_add_u32 s8, s90, s8
	v_lshlrev_b32_e32 v52, 2, v0
	v_lshlrev_b32_e32 v0, 3, v194
	v_mov_b32_e32 v1, v5
	s_addc_u32 s9, s91, s9
	v_lshl_add_u64 v[0:1], s[8:9], 0, v[0:1]
	s_mov_b64 s[8:9], 0x10000000
	s_ashr_i32 s5, s4, 31
	v_lshl_add_u64 v[16:17], v[0:1], 0, s[8:9]
	s_lshl_b64 s[8:9], s[4:5], 12
	s_lshl_b64 s[20:21], s[2:3], 13
	s_add_u32 s20, s88, s20
	s_addc_u32 s21, s89, s21
	s_mov_b64 s[10:11], 0x1000
	v_lshl_add_u64 v[0:1], s[20:21], 0, v[4:5]
	v_lshl_add_u64 v[8:9], v[6:7], 0, s[10:11]
	v_lshl_add_u64 v[18:19], v[0:1], 0, s[10:11]
	s_lshl_b64 s[10:11], s[4:5], 13
	s_add_i32 s3, 0, 0x22020
	v_lshlrev_b32_e32 v53, 2, v194
	v_mov_b32_e32 v54, 0x358637bd
	s_mov_b32 s5, 0x800000
	global_load_dwordx4 v[196:199], v[6:7], off
	global_load_dwordx4 v[200:203], v[6:7], off offset:1024
	global_load_dwordx4 v[204:207], v[6:7], off offset:2048
	global_load_dwordx4 v[208:211], v[6:7], off offset:3072
	global_load_dwordx4 v[212:215], v[8:9], off
	global_load_dwordx4 v[216:219], v[10:11], off
	global_load_dwordx4 v[220:223], v[12:13], off
	global_load_dwordx4 v[224:227], v[14:15], off
	s_ashr_i32 s7, s6, 31
	s_lshl_b64 s[20:21], s[6:7], 2
	s_add_u32 s22, s12, s20
	s_addc_u32 s23, s13, s21
	global_load_dwordx4 v[236:239], v5, s[22:23]
	s_add_u32 s22, s14, s20
	s_addc_u32 s23, s15, s21
	s_add_u32 s20, s16, s20
	s_addc_u32 s21, s17, s21
	global_load_dword v240, v5, s[22:23]
	global_load_dword v241, v5, s[20:21]
	s_add_i32 s22, s6, 1
	s_ashr_i32 s23, s22, 31
	s_lshl_b64 s[20:21], s[22:23], 2
	s_add_u32 s22, s14, s20
	s_addc_u32 s23, s15, s21
	global_load_dwordx3 v[242:244], v5, s[22:23]
	s_add_u32 s20, s16, s20
	s_addc_u32 s21, s17, s21
	global_load_dword v245, v5, s[20:21]
	s_add_i32 s22, s6, 2
	s_ashr_i32 s23, s22, 31
	s_lshl_b64 s[20:21], s[22:23], 2
	s_add_u32 s20, s16, s20
	s_addc_u32 s21, s17, s21
	global_load_dwordx2 v[246:247], v5, s[20:21]
	s_add_i32 s6, s6, s18
	s_waitcnt vmcnt(0)
.LBB0_1128:
	s_ashr_i32 s7, s6, 31
	s_lshl_b64 s[20:21], s[6:7], 2
	s_add_u32 s22, s12, s20
	s_addc_u32 s23, s13, s21
	global_load_dwordx2 v[36:37], v[16:17], off
	global_load_dwordx2 v[40:41], v[16:17], off offset:512
	global_load_dwordx2 v[42:43], v[16:17], off offset:1024
	global_load_dwordx2 v[34:35], v[16:17], off offset:1536
	global_load_dwordx2 v[30:31], v[16:17], off offset:2048
	global_load_dwordx2 v[26:27], v[16:17], off offset:2560
	global_load_dwordx2 v[22:23], v[16:17], off offset:3072
	global_load_dwordx2 v[20:21], v[16:17], off offset:3584
	v_mov_b32_e32 v56, v236
	v_mov_b32_e32 v57, v237
	v_mov_b32_e32 v58, v238
	v_mov_b32_e32 v59, v239
	v_mov_b32_e32 v64, v240
	v_mov_b32_e32 v28, v241
	v_mov_b32_e32 v60, v242
	v_mov_b32_e32 v61, v243
	v_mov_b32_e32 v62, v244
	v_mov_b32_e32 v4, v245
	v_mov_b32_e32 v24, v246
	v_mov_b32_e32 v25, v247
	global_load_dwordx4 v[236:239], v5, s[22:23]
	s_add_u32 s22, s14, s20
	s_addc_u32 s23, s15, s21
	s_add_u32 s20, s16, s20
	s_addc_u32 s21, s17, s21
	global_load_dword v240, v5, s[22:23]
	global_load_dword v241, v5, s[20:21]
	s_add_i32 s22, s6, 1
	s_ashr_i32 s23, s22, 31
	s_lshl_b64 s[20:21], s[22:23], 2
	s_add_u32 s22, s14, s20
	s_addc_u32 s23, s15, s21
	global_load_dwordx3 v[242:244], v5, s[22:23]
	s_add_u32 s20, s16, s20
	s_addc_u32 s21, s17, s21
	global_load_dword v245, v5, s[20:21]
	s_add_i32 s22, s6, 2
	s_ashr_i32 s23, s22, 31
	s_lshl_b64 s[20:21], s[22:23], 2
	s_add_u32 s20, s16, s20
	s_addc_u32 s21, s17, s21
	global_load_dwordx2 v[246:247], v5, s[20:21]
	s_add_i32 s2, s2, s4
	s_add_i32 s6, s6, s18
	v_lshl_add_u64 v[16:17], v[16:17], 0, s[8:9]
	s_cmpk_lt_i32 s2, 0x2000


; __device__ __forceinline__ float bf_lo(unsigned u) { return __uint_as_float(u << 16); }
; __device__ __forceinline__ float bf_hi(unsigned u) { return __uint_as_float(u & 0xffff0000u); }
; __device__ __forceinline__ void p9_final(Ctx& X) {
;     ...
;         for (int j = 0; j < 8; ++j) { const u32x2 hv = hr[64 * j]; v[j] = (f32x4){bf_lo(hv.x), bf_hi(hv.x), bf_lo(hv.y), bf_hi(hv.y)}; }
; #pragma unroll
;         for (int k = 0; k < 4; ++k) { const int e = XP_TOPI(X)[t * 4 + k], r = XP_TOPR(X)[t * 4 + k]; const float wk = XP_TOPW(X)[t * 4 + k];
;             const unsigned* yr = (const unsigned*)(XP_YR(X) + ((size_t)tab[8 + e] * 256 + r) * D) + lane;
; #pragma unroll
;             for (int j = 0; j < 8; ++j) { const int y = (int)yr[64 * j]; const f32x2 lo = __builtin_amdgcn_cvt_pk_f32_fp8(y, false), hi = __builtin_amdgcn_cvt_pk_f32_fp8(y, true);
;                 v[j].x += wk * lo.x; v[j].y += wk * lo.y; v[j].z += wk * hi.x; v[j].w += wk * hi.y; } }
	v_lshlrev_b32_e32 v55, 2, v56
	v_lshlrev_b32_e32 v56, 2, v57
	v_lshlrev_b32_e32 v57, 2, v58
	v_lshlrev_b32_e32 v58, 2, v59
	v_add_u32_e32 v55, s3, v55
	v_add_u32_e32 v59, s3, v56
	v_add_u32_e32 v57, s3, v57
	v_add_u32_e32 v63, s3, v58
	ds_read_b32 v56, v55
	ds_read_b32 v58, v59
	ds_read_b32 v74, v57
	ds_read_b32 v76, v63
	v_ashrrev_i32_e32 v65, 31, v64
	s_waitcnt lgkmcnt(3)
	v_ashrrev_i32_e32 v57, 31, v56
	s_waitcnt lgkmcnt(2)
	v_ashrrev_i32_e32 v59, 31, v58
	s_waitcnt lgkmcnt(1)
	v_ashrrev_i32_e32 v75, 31, v74
	s_waitcnt lgkmcnt(0)
	v_ashrrev_i32_e32 v77, 31, v76
	v_lshlrev_b64 v[56:57], 19, v[56:57]
	v_lshlrev_b64 v[64:65], 11, v[64:65]
	v_ashrrev_i32_e32 v79, 31, v60
	v_mov_b32_e32 v78, v60
	v_lshlrev_b64 v[58:59], 19, v[58:59]
	v_ashrrev_i32_e32 v81, 31, v61
	v_mov_b32_e32 v80, v61
	v_lshlrev_b64 v[60:61], 19, v[74:75]
	v_ashrrev_i32_e32 v63, 31, v62
	v_lshlrev_b64 v[74:75], 19, v[76:77]
	v_lshl_add_u64 v[56:57], s[0:1], 0, v[56:57]
	v_lshlrev_b64 v[76:77], 11, v[78:79]
	v_lshl_add_u64 v[58:59], s[0:1], 0, v[58:59]
	v_lshlrev_b64 v[78:79], 11, v[80:81]
	v_lshl_add_u64 v[60:61], s[0:1], 0, v[60:61]
	v_lshlrev_b64 v[62:63], 11, v[62:63]
	v_lshl_add_u64 v[74:75], s[0:1], 0, v[74:75]
	v_lshl_add_u64 v[56:57], v[56:57], 0, v[64:65]
	v_lshl_add_u64 v[58:59], v[58:59], 0, v[76:77]
	v_lshl_add_u64 v[60:61], v[60:61], 0, v[78:79]
	v_lshl_add_u64 v[62:63], v[74:75], 0, v[62:63]
	v_readfirstlane_b32 s20, v56
	v_readfirstlane_b32 s21, v57
	v_readfirstlane_b32 s22, v58
	v_readfirstlane_b32 s23, v59
	v_readfirstlane_b32 s24, v60
	v_readfirstlane_b32 s25, v61
	v_readfirstlane_b32 s26, v62
	v_readfirstlane_b32 s27, v63
	global_load_dword v55, v53, s[20:21]
	global_load_dword v62, v53, s[20:21] offset:256
	global_load_dword v74, v53, s[20:21] offset:512
	global_load_dword v78, v53, s[20:21] offset:768
	global_load_dword v82, v53, s[20:21] offset:1024
	global_load_dword v86, v53, s[20:21] offset:1280
	global_load_dword v90, v53, s[20:21] offset:1536
	global_load_dword v94, v53, s[20:21] offset:1792
	global_load_dword v98, v53, s[22:23]
	global_load_dword v102, v53, s[22:23] offset:256
	global_load_dword v106, v53, s[22:23] offset:512
	global_load_dword v110, v53, s[22:23] offset:768
	global_load_dword v114, v53, s[22:23] offset:1024
	global_load_dword v118, v53, s[22:23] offset:1280
	global_load_dword v122, v53, s[22:23] offset:1536
	global_load_dword v126, v53, s[22:23] offset:1792
	global_load_dword v130, v53, s[24:25]
	global_load_dword v134, v53, s[24:25] offset:256
	global_load_dword v138, v53, s[24:25] offset:512
	global_load_dword v142, v53, s[24:25] offset:768
	global_load_dword v146, v53, s[24:25] offset:1024
	global_load_dword v150, v53, s[24:25] offset:1280
	global_load_dword v154, v53, s[24:25] offset:1536
	global_load_dword v158, v53, s[24:25] offset:1792
	global_load_dword v162, v53, s[26:27]
	global_load_dword v166, v53, s[26:27] offset:256
	global_load_dword v170, v53, s[26:27] offset:512
	global_load_dword v174, v53, s[26:27] offset:768
	global_load_dword v178, v53, s[26:27] offset:1024
	global_load_dword v182, v53, s[26:27] offset:1280
	global_load_dword v186, v53, s[26:27] offset:1536
	global_load_dword v190, v53, s[26:27] offset:1792
	s_waitcnt vmcnt(32)
	v_lshlrev_b32_e32 v32, 16, v36
	v_and_b32_e32 v33, 0xffff0000, v36
	v_lshlrev_b32_e32 v36, 16, v37
	v_and_b32_e32 v37, 0xffff0000, v37
	v_lshlrev_b32_e32 v38, 16, v40
	v_and_b32_e32 v39, 0xffff0000, v40
	v_lshlrev_b32_e32 v40, 16, v41
	v_and_b32_e32 v41, 0xffff0000, v41
	v_lshlrev_b32_e32 v44, 16, v42
	v_and_b32_e32 v45, 0xffff0000, v42
	v_lshlrev_b32_e32 v42, 16, v43
	v_and_b32_e32 v43, 0xffff0000, v43
	v_lshlrev_b32_e32 v46, 16, v34
	v_and_b32_e32 v47, 0xffff0000, v34
	v_lshlrev_b32_e32 v34, 16, v35
	v_and_b32_e32 v35, 0xffff0000, v35
	v_lshlrev_b32_e32 v66, 16, v30
	v_and_b32_e32 v67, 0xffff0000, v30
	v_lshlrev_b32_e32 v30, 16, v31
	v_and_b32_e32 v31, 0xffff0000, v31
	v_lshlrev_b32_e32 v68, 16, v26
	v_and_b32_e32 v69, 0xffff0000, v26
	v_lshlrev_b32_e32 v26, 16, v27
	v_and_b32_e32 v27, 0xffff0000, v27
	v_lshlrev_b32_e32 v70, 16, v22
	v_and_b32_e32 v71, 0xffff0000, v22
	v_lshlrev_b32_e32 v22, 16, v23
	v_and_b32_e32 v23, 0xffff0000, v23
	v_lshlrev_b32_e32 v72, 16, v20
	v_and_b32_e32 v73, 0xffff0000, v20
	v_lshlrev_b32_e32 v20, 16, v21
	v_and_b32_e32 v21, 0xffff0000, v21
	s_waitcnt vmcnt(31)
	v_cvt_pk_f32_fp8_e32 v[56:57], v55
	v_cvt_pk_f32_fp8_sdwa v[58:59], v55 src0_sel:WORD_1
	s_waitcnt vmcnt(30)
	v_cvt_pk_f32_fp8_e32 v[60:61], v62
	v_cvt_pk_f32_fp8_sdwa v[62:63], v62 src0_sel:WORD_1
	s_waitcnt vmcnt(29)
	v_cvt_pk_f32_fp8_e32 v[64:65], v74
	v_cvt_pk_f32_fp8_sdwa v[74:75], v74 src0_sel:WORD_1
	s_waitcnt vmcnt(28)
	v_cvt_pk_f32_fp8_e32 v[76:77], v78
	v_cvt_pk_f32_fp8_sdwa v[78:79], v78 src0_sel:WORD_1
	s_waitcnt vmcnt(23)
	v_cvt_pk_f32_fp8_e32 v[96:97], v98
	v_cvt_pk_f32_fp8_sdwa v[98:99], v98 src0_sel:WORD_1
	s_waitcnt vmcnt(22)
	v_cvt_pk_f32_fp8_e32 v[100:101], v102
	v_cvt_pk_f32_fp8_sdwa v[102:103], v102 src0_sel:WORD_1
	v_cvt_pk_f32_fp8_e32 v[80:81], v82
	v_cvt_pk_f32_fp8_sdwa v[82:83], v82 src0_sel:WORD_1
	v_cvt_pk_f32_fp8_e32 v[84:85], v86
	v_cvt_pk_f32_fp8_sdwa v[86:87], v86 src0_sel:WORD_1
	v_cvt_pk_f32_fp8_e32 v[88:89], v90
	v_cvt_pk_f32_fp8_sdwa v[90:91], v90 src0_sel:WORD_1
	v_cvt_pk_f32_fp8_e32 v[92:93], v94
	v_cvt_pk_f32_fp8_sdwa v[94:95], v94 src0_sel:WORD_1
	s_waitcnt vmcnt(21)
	v_cvt_pk_f32_fp8_e32 v[104:105], v106
	v_cvt_pk_f32_fp8_sdwa v[106:107], v106 src0_sel:WORD_1
	s_waitcnt vmcnt(15)
	v_cvt_pk_f32_fp8_e32 v[128:129], v130
	v_cvt_pk_f32_fp8_sdwa v[130:131], v130 src0_sel:WORD_1
	s_waitcnt vmcnt(14)
; __device__ __forceinline__ void p9_final(Ctx& X) {
;     ...
;             for (int j = 0; j < 8; ++j) { const int y = (int)yr[64 * j]; const f32x2 lo = __builtin_amdgcn_cvt_pk_f32_fp8(y, false), hi = __builtin_amdgcn_cvt_pk_f32_fp8(y, true);
;                 v[j].x += wk * lo.x; v[j].y += wk * lo.y; v[j].z += wk * hi.x; v[j].w += wk * hi.y; } }
	v_cvt_pk_f32_fp8_e32 v[132:133], v134
	v_cvt_pk_f32_fp8_sdwa v[134:135], v134 src0_sel:WORD_1
	v_cvt_pk_f32_fp8_e32 v[108:109], v110
	v_cvt_pk_f32_fp8_sdwa v[110:111], v110 src0_sel:WORD_1
	v_cvt_pk_f32_fp8_e32 v[112:113], v114
	v_cvt_pk_f32_fp8_sdwa v[114:115], v114 src0_sel:WORD_1
	v_cvt_pk_f32_fp8_e32 v[116:117], v118
	v_cvt_pk_f32_fp8_sdwa v[118:119], v118 src0_sel:WORD_1
	v_cvt_pk_f32_fp8_e32 v[120:121], v122
	v_cvt_pk_f32_fp8_sdwa v[122:123], v122 src0_sel:WORD_1
	v_cvt_pk_f32_fp8_e32 v[124:125], v126
	v_cvt_pk_f32_fp8_sdwa v[126:127], v126 src0_sel:WORD_1
	s_waitcnt vmcnt(13)
	v_cvt_pk_f32_fp8_e32 v[136:137], v138
	v_cvt_pk_f32_fp8_sdwa v[138:139], v138 src0_sel:WORD_1
	s_waitcnt vmcnt(7)
	v_cvt_pk_f32_fp8_e32 v[160:161], v162
	v_cvt_pk_f32_fp8_sdwa v[162:163], v162 src0_sel:WORD_1
	s_waitcnt vmcnt(6)
	v_cvt_pk_f32_fp8_e32 v[164:165], v166
	v_cvt_pk_f32_fp8_sdwa v[166:167], v166 src0_sel:WORD_1
	v_cvt_pk_f32_fp8_e32 v[140:141], v142
	v_cvt_pk_f32_fp8_sdwa v[142:143], v142 src0_sel:WORD_1
	v_cvt_pk_f32_fp8_e32 v[144:145], v146
	v_cvt_pk_f32_fp8_sdwa v[146:147], v146 src0_sel:WORD_1
	v_cvt_pk_f32_fp8_e32 v[148:149], v150
	v_cvt_pk_f32_fp8_sdwa v[150:151], v150 src0_sel:WORD_1
	v_cvt_pk_f32_fp8_e32 v[152:153], v154
	v_cvt_pk_f32_fp8_sdwa v[154:155], v154 src0_sel:WORD_1
	v_cvt_pk_f32_fp8_e32 v[156:157], v158
	v_cvt_pk_f32_fp8_sdwa v[158:159], v158 src0_sel:WORD_1
	s_waitcnt vmcnt(5)
	v_cvt_pk_f32_fp8_e32 v[168:169], v170
	v_cvt_pk_f32_fp8_sdwa v[170:171], v170 src0_sel:WORD_1
	v_pk_fma_f32 v[32:33], v[28:29], v[56:57], v[32:33] op_sel_hi:[0,1,1]
	v_pk_fma_f32 v[36:37], v[28:29], v[58:59], v[36:37] op_sel_hi:[0,1,1]
	v_pk_fma_f32 v[38:39], v[28:29], v[60:61], v[38:39] op_sel_hi:[0,1,1]
	v_pk_fma_f32 v[40:41], v[28:29], v[62:63], v[40:41] op_sel_hi:[0,1,1]
	s_waitcnt vmcnt(4)
	v_cvt_pk_f32_fp8_e32 v[172:173], v174
	v_cvt_pk_f32_fp8_sdwa v[174:175], v174 src0_sel:WORD_1
	s_waitcnt vmcnt(3)
	v_cvt_pk_f32_fp8_e32 v[176:177], v178
	v_cvt_pk_f32_fp8_sdwa v[178:179], v178 src0_sel:WORD_1
	s_waitcnt vmcnt(2)
	v_cvt_pk_f32_fp8_e32 v[180:181], v182
	v_cvt_pk_f32_fp8_sdwa v[182:183], v182 src0_sel:WORD_1
	s_waitcnt vmcnt(1)
	v_cvt_pk_f32_fp8_e32 v[184:185], v186
	v_cvt_pk_f32_fp8_sdwa v[186:187], v186 src0_sel:WORD_1
	s_waitcnt vmcnt(0)
	v_cvt_pk_f32_fp8_e32 v[188:189], v190
	v_cvt_pk_f32_fp8_sdwa v[190:191], v190 src0_sel:WORD_1
	v_pk_fma_f32 v[44:45], v[28:29], v[64:65], v[44:45] op_sel_hi:[0,1,1]
	v_pk_fma_f32 v[42:43], v[28:29], v[74:75], v[42:43] op_sel_hi:[0,1,1]
	v_pk_fma_f32 v[32:33], v[4:5], v[96:97], v[32:33] op_sel_hi:[0,1,1]
	v_pk_fma_f32 v[36:37], v[4:5], v[98:99], v[36:37] op_sel_hi:[0,1,1]
	v_pk_fma_f32 v[38:39], v[4:5], v[100:101], v[38:39] op_sel_hi:[0,1,1]
	v_pk_fma_f32 v[40:41], v[4:5], v[102:103], v[40:41] op_sel_hi:[0,1,1]
	v_pk_fma_f32 v[46:47], v[28:29], v[76:77], v[46:47] op_sel_hi:[0,1,1]
	v_pk_fma_f32 v[34:35], v[28:29], v[78:79], v[34:35] op_sel_hi:[0,1,1]
	v_pk_fma_f32 v[56:57], v[28:29], v[80:81], v[66:67] op_sel_hi:[0,1,1]
	v_pk_fma_f32 v[30:31], v[28:29], v[82:83], v[30:31] op_sel_hi:[0,1,1]
	v_pk_fma_f32 v[58:59], v[28:29], v[84:85], v[68:69] op_sel_hi:[0,1,1]
	v_pk_fma_f32 v[26:27], v[28:29], v[86:87], v[26:27] op_sel_hi:[0,1,1]
	v_pk_fma_f32 v[60:61], v[28:29], v[88:89], v[70:71] op_sel_hi:[0,1,1]
	v_pk_fma_f32 v[22:23], v[28:29], v[90:91], v[22:23] op_sel_hi:[0,1,1]
	v_pk_fma_f32 v[62:63], v[28:29], v[92:93], v[72:73] op_sel_hi:[0,1,1]
	v_pk_fma_f32 v[20:21], v[28:29], v[94:95], v[20:21] op_sel_hi:[0,1,1]
	v_pk_fma_f32 v[44:45], v[4:5], v[104:105], v[44:45] op_sel_hi:[0,1,1]
	v_pk_fma_f32 v[42:43], v[4:5], v[106:107], v[42:43] op_sel_hi:[0,1,1]
	v_pk_fma_f32 v[32:33], v[24:25], v[128:129], v[32:33] op_sel_hi:[0,1,1]
	v_pk_fma_f32 v[36:37], v[24:25], v[130:131], v[36:37] op_sel_hi:[0,1,1]
	v_pk_fma_f32 v[38:39], v[24:25], v[132:133], v[38:39] op_sel_hi:[0,1,1]
	v_pk_fma_f32 v[40:41], v[24:25], v[134:135], v[40:41] op_sel_hi:[0,1,1]
	v_pk_fma_f32 v[46:47], v[4:5], v[108:109], v[46:47] op_sel_hi:[0,1,1]
	v_pk_fma_f32 v[34:35], v[4:5], v[110:111], v[34:35] op_sel_hi:[0,1,1]
	v_pk_fma_f32 v[56:57], v[4:5], v[112:113], v[56:57] op_sel_hi:[0,1,1]
	v_pk_fma_f32 v[30:31], v[4:5], v[114:115], v[30:31] op_sel_hi:[0,1,1]
	v_pk_fma_f32 v[58:59], v[4:5], v[116:117], v[58:59] op_sel_hi:[0,1,1]
	v_pk_fma_f32 v[26:27], v[4:5], v[118:119], v[26:27] op_sel_hi:[0,1,1]
	v_pk_fma_f32 v[60:61], v[4:5], v[120:121], v[60:61] op_sel_hi:[0,1,1]
	v_pk_fma_f32 v[22:23], v[4:5], v[122:123], v[22:23] op_sel_hi:[0,1,1]
	v_pk_fma_f32 v[62:63], v[4:5], v[124:125], v[62:63] op_sel_hi:[0,1,1]
	v_pk_fma_f32 v[20:21], v[4:5], v[126:127], v[20:21] op_sel_hi:[0,1,1]
	v_pk_fma_f32 v[44:45], v[24:25], v[136:137], v[44:45] op_sel_hi:[0,1,1]
	v_pk_fma_f32 v[42:43], v[24:25], v[138:139], v[42:43] op_sel_hi:[0,1,1]
	v_pk_fma_f32 v[32:33], v[24:25], v[160:161], v[32:33] op_sel:[1,0,0]
	v_pk_fma_f32 v[36:37], v[24:25], v[162:163], v[36:37] op_sel:[1,0,0]
	v_pk_fma_f32 v[38:39], v[24:25], v[164:165], v[38:39] op_sel:[1,0,0]
	v_pk_fma_f32 v[40:41], v[24:25], v[166:167], v[40:41] op_sel:[1,0,0]
	v_pk_fma_f32 v[46:47], v[24:25], v[140:141], v[46:47] op_sel_hi:[0,1,1]
	v_pk_fma_f32 v[34:35], v[24:25], v[142:143], v[34:35] op_sel_hi:[0,1,1]
	v_pk_fma_f32 v[56:57], v[24:25], v[144:145], v[56:57] op_sel_hi:[0,1,1]
	v_pk_fma_f32 v[30:31], v[24:25], v[146:147], v[30:31] op_sel_hi:[0,1,1]
	v_pk_fma_f32 v[58:59], v[24:25], v[148:149], v[58:59] op_sel_hi:[0,1,1]
	v_pk_fma_f32 v[26:27], v[24:25], v[150:151], v[26:27] op_sel_hi:[0,1,1]
	v_pk_fma_f32 v[60:61], v[24:25], v[152:153], v[60:61] op_sel_hi:[0,1,1]
	v_pk_fma_f32 v[22:23], v[24:25], v[154:155], v[22:23] op_sel_hi:[0,1,1]
; __device__ __forceinline__ void p9_final(Ctx& X) {
;     ...
;         float s = 0.f;
; #pragma unroll
;         for (int j = 0; j < 8; ++j) s += (v[j].x * v[j].x + v[j].y * v[j].y) + (v[j].z * v[j].z + v[j].w * v[j].w);
;         const float rstd = rsqrtf(wave_sum(s) * (1.f / D) + EPS);
;         f32x4* o = (f32x4*)(X.out + (size_t)t * D) + lane; const f32x4* wr_ = (const f32x4*)XP_ln_final_w(X) + lane;
; #pragma unroll
;         for (int j = 0; j < 8; ++j) { const f32x4 wv = wr_[64 * j]; f32x4 r; r.x = v[j].x * rstd * wv.x; r.y = v[j].y * rstd * wv.y; r.z = v[j].z * rstd * wv.z; r.w = v[j].w * rstd * wv.w; __builtin_nontemporal_store(r, &o[64 * j]); }
;     }
	v_pk_fma_f32 v[62:63], v[24:25], v[156:157], v[62:63] op_sel_hi:[0,1,1]
	v_pk_fma_f32 v[20:21], v[24:25], v[158:159], v[20:21] op_sel_hi:[0,1,1]
	v_pk_fma_f32 v[44:45], v[24:25], v[168:169], v[44:45] op_sel:[1,0,0]
	v_pk_fma_f32 v[42:43], v[24:25], v[170:171], v[42:43] op_sel:[1,0,0]
	v_mov_b32_e32 v64, v33
	v_mov_b32_e32 v65, v39
	v_mov_b32_e32 v68, v37
	v_mov_b32_e32 v69, v41
	v_pk_fma_f32 v[46:47], v[24:25], v[172:173], v[46:47] op_sel:[1,0,0]
	v_pk_fma_f32 v[34:35], v[24:25], v[174:175], v[34:35] op_sel:[1,0,0]
	v_pk_fma_f32 v[56:57], v[24:25], v[176:177], v[56:57] op_sel:[1,0,0]
	v_pk_fma_f32 v[30:31], v[24:25], v[178:179], v[30:31] op_sel:[1,0,0]
	v_pk_fma_f32 v[58:59], v[24:25], v[180:181], v[58:59] op_sel:[1,0,0]
	v_pk_fma_f32 v[26:27], v[24:25], v[182:183], v[26:27] op_sel:[1,0,0]
	v_pk_fma_f32 v[60:61], v[24:25], v[184:185], v[60:61] op_sel:[1,0,0]
	v_pk_fma_f32 v[22:23], v[24:25], v[186:187], v[22:23] op_sel:[1,0,0]
	v_pk_fma_f32 v[62:63], v[24:25], v[188:189], v[62:63] op_sel:[1,0,0]
	v_pk_fma_f32 v[20:21], v[24:25], v[190:191], v[20:21] op_sel:[1,0,0]
	v_mov_b32_e32 v24, v32
	v_mov_b32_e32 v25, v38
	v_mov_b32_e32 v66, v36
	v_mov_b32_e32 v67, v40
	v_mov_b32_e32 v72, v45
	v_mov_b32_e32 v73, v43
	v_pk_mul_f32 v[64:65], v[64:65], v[64:65]
	v_pk_mul_f32 v[68:69], v[68:69], v[68:69]
	v_mov_b32_e32 v70, v44
	v_mov_b32_e32 v71, v42
	v_pk_mul_f32 v[72:73], v[72:73], v[72:73]
	v_pk_fma_f32 v[24:25], v[24:25], v[24:25], v[64:65]
	v_pk_fma_f32 v[64:65], v[66:67], v[66:67], v[68:69]
	v_mul_f32_e32 v4, v47, v47
	v_mul_f32_e32 v28, v35, v35
	v_pk_fma_f32 v[66:67], v[70:71], v[70:71], v[72:73]
	v_pk_add_f32 v[24:25], v[24:25], v[64:65]
	v_pk_mul_f32 v[74:75], v[56:57], v[56:57]
	v_pk_mul_f32 v[76:77], v[30:31], v[30:31]
	v_pk_fma_f32 v[90:91], v[46:47], v[46:47], v[4:5] op_sel_hi:[1,1,0]
	v_pk_fma_f32 v[92:93], v[34:35], v[34:35], v[28:29] op_sel_hi:[1,1,0]
	v_pk_add_f32 v[64:65], v[66:67], v[66:67] op_sel:[0,1] op_sel_hi:[1,0]
	v_pk_add_f32 v[24:25], v[24:25], v[24:25] op_sel:[0,1] op_sel_hi:[1,0]
	v_mov_b32_e32 v80, v59
	v_mov_b32_e32 v81, v27
	v_mov_b32_e32 v91, v76
	v_mov_b32_e32 v93, v77
	v_mov_b32_e32 v65, v75
	v_mov_b32_e32 v25, v74
	v_mov_b32_e32 v78, v58
	v_mov_b32_e32 v79, v26
	v_pk_mul_f32 v[80:81], v[80:81], v[80:81]
	v_pk_add_f32 v[66:67], v[90:91], v[92:93]
	v_pk_add_f32 v[24:25], v[24:25], v[64:65]
	v_mul_f32_e32 v82, v61, v61
	v_mul_f32_e32 v84, v23, v23
	v_pk_fma_f32 v[68:69], v[78:79], v[78:79], v[80:81]
	v_pk_add_f32 v[24:25], v[24:25], v[66:67]
	v_pk_mul_f32 v[86:87], v[62:63], v[62:63]
	v_pk_mul_f32 v[88:89], v[20:21], v[20:21]
	v_pk_fma_f32 v[82:83], v[60:61], v[60:61], v[82:83] op_sel_hi:[1,1,0]
	v_pk_fma_f32 v[84:85], v[22:23], v[22:23], v[84:85] op_sel_hi:[1,1,0]
	v_pk_add_f32 v[68:69], v[68:69], v[68:69] op_sel:[0,1] op_sel_hi:[1,0]
	v_pk_add_f32 v[24:25], v[24:25], v[24:25] op_sel:[0,1] op_sel_hi:[1,0]
	v_mov_b32_e32 v83, v88
	v_mov_b32_e32 v85, v89
	v_mov_b32_e32 v69, v87
	v_mov_b32_e32 v25, v86
	v_pk_add_f32 v[70:71], v[82:83], v[84:85]
	v_pk_add_f32 v[24:25], v[24:25], v[68:69]
	s_nop 0
	v_pk_add_f32 v[24:25], v[24:25], v[70:71]
	s_nop 0
	v_add_f32_e32 v4, v24, v25
	ds_bpermute_b32 v24, v29, v4
	s_waitcnt lgkmcnt(0)
	v_add_f32_e32 v4, v4, v24
	ds_bpermute_b32 v24, v48, v4
	s_waitcnt lgkmcnt(0)
	v_add_f32_e32 v4, v4, v24
	ds_bpermute_b32 v24, v49, v4
	s_waitcnt lgkmcnt(0)
	v_add_f32_e32 v4, v4, v24
	ds_bpermute_b32 v24, v50, v4
	s_waitcnt lgkmcnt(0)
	v_add_f32_e32 v4, v4, v24
	ds_bpermute_b32 v24, v51, v4
	s_waitcnt lgkmcnt(0)
	v_add_f32_e32 v4, v4, v24
	ds_bpermute_b32 v24, v52, v4
	s_waitcnt lgkmcnt(0)
	v_add_f32_e32 v4, v4, v24
	v_fmamk_f32 v4, v4, 0x3a000000, v54
	v_mul_f32_e32 v24, 0x4b800000, v4
	v_cmp_gt_f32_e32 vcc, s5, v4
	s_nop 1
	v_cndmask_b32_e32 v4, v4, v24, vcc
	v_rsq_f32_e32 v4, v4
	s_nop 0
	v_mul_f32_e32 v24, 0x45800000, v4
	v_cndmask_b32_e32 v4, v4, v24, vcc
	v_pk_mul_f32 v[24:25], v[32:33], v[4:5] op_sel_hi:[1,0]
	v_pk_mul_f32 v[32:33], v[36:37], v[4:5] op_sel_hi:[1,0]
	v_pk_mul_f32 v[228:229], v[196:197], v[24:25]
	v_pk_mul_f32 v[230:231], v[198:199], v[32:33]
	global_store_dwordx4 v[18:19], v[228:231], off offset:-4096 nt
	v_pk_mul_f32 v[24:25], v[40:41], v[4:5] op_sel_hi:[1,0]
	v_pk_mul_f32 v[32:33], v[38:39], v[4:5] op_sel_hi:[1,0]
	v_pk_mul_f32 v[22:23], v[22:23], v[4:5] op_sel_hi:[1,0]
	v_pk_mul_f32 v[20:21], v[20:21], v[4:5] op_sel_hi:[1,0]
	v_pk_mul_f32 v[232:233], v[200:201], v[32:33]
	v_pk_mul_f32 v[234:235], v[202:203], v[24:25]
	global_store_dwordx4 v[18:19], v[232:235], off offset:-3072 nt
	v_pk_mul_f32 v[24:25], v[42:43], v[4:5] op_sel_hi:[1,0]
	v_pk_mul_f32 v[32:33], v[44:45], v[4:5] op_sel_hi:[1,0]
	v_pk_mul_f32 v[230:231], v[206:207], v[24:25]
	v_pk_mul_f32 v[228:229], v[204:205], v[32:33]
	global_store_dwordx4 v[18:19], v[228:231], off offset:-2048 nt
	v_pk_mul_f32 v[24:25], v[34:35], v[4:5] op_sel_hi:[1,0]
	v_pk_mul_f32 v[32:33], v[46:47], v[4:5] op_sel_hi:[1,0]
	v_pk_mul_f32 v[234:235], v[210:211], v[24:25]
	v_pk_mul_f32 v[232:233], v[208:209], v[32:33]
	global_store_dwordx4 v[18:19], v[232:235], off offset:-1024 nt
	v_pk_mul_f32 v[24:25], v[30:31], v[4:5] op_sel_hi:[1,0]
	v_pk_mul_f32 v[30:31], v[56:57], v[4:5] op_sel_hi:[1,0]
	v_pk_mul_f32 v[230:231], v[214:215], v[24:25]
	v_pk_mul_f32 v[228:229], v[212:213], v[30:31]
	global_store_dwordx4 v[18:19], v[228:231], off nt
	v_pk_mul_f32 v[24:25], v[26:27], v[4:5] op_sel_hi:[1,0]
	v_pk_mul_f32 v[26:27], v[58:59], v[4:5] op_sel_hi:[1,0]
	v_pk_mul_f32 v[234:235], v[218:219], v[24:25]
	v_pk_mul_f32 v[232:233], v[216:217], v[26:27]
	global_store_dwordx4 v[18:19], v[232:235], off offset:1024 nt
	v_pk_mul_f32 v[24:25], v[60:61], v[4:5] op_sel_hi:[1,0]
	v_pk_mul_f32 v[230:231], v[22:23], v[222:223]
	v_pk_mul_f32 v[228:229], v[24:25], v[220:221]
	global_store_dwordx4 v[18:19], v[228:231], off offset:2048 nt
	v_pk_mul_f32 v[22:23], v[62:63], v[4:5] op_sel_hi:[1,0]
	v_pk_mul_f32 v[234:235], v[20:21], v[226:227]
	v_pk_mul_f32 v[232:233], v[22:23], v[224:225]
	global_store_dwordx4 v[18:19], v[232:235], off offset:3072 nt
	v_lshl_add_u64 v[18:19], v[18:19], 0, s[10:11]
	s_cbranch_scc1 .LBB0_1128
